# v73 stack + grid barrier: L1 invalidate issued at arrival (before polling / with the L2 write-back) instead of after the release
# baseline (speedup 1.0000x reference)
.LBB0_42:
	s_or_b64 exec, exec, s[6:7]
	v_cvt_f32_u32_e32 v4, v2
	s_waitcnt vmcnt(0)
	v_readfirstlane_b32 s4, v3
	v_sub_u32_e32 v3, 0, v2
	v_rcp_iflag_f32_e32 v4, v4
	v_add_u32_e32 v5, s4, v1
	v_mul_f32_e32 v4, 0x4f7ffffe, v4
	v_cvt_u32_f32_e32 v4, v4
	v_mul_lo_u32 v1, v3, v4
	v_mul_hi_u32 v1, v4, v1
	v_add_u32_e32 v1, v4, v1
	v_mul_hi_u32 v1, v5, v1
	v_mul_lo_u32 v3, v1, v2
	v_sub_u32_e32 v3, v5, v3
	v_add_u32_e32 v4, 1, v1
	v_cmp_ge_u32_e32 vcc, v3, v2
	s_nop 1
	v_cndmask_b32_e32 v1, v1, v4, vcc
	v_sub_u32_e32 v4, v3, v2
	v_cndmask_b32_e32 v3, v3, v4, vcc
	v_add_u32_e32 v4, 1, v1
	v_cmp_ge_u32_e32 vcc, v3, v2
	v_add_u32_e32 v3, 1, v5
	s_nop 0
	v_cndmask_b32_e32 v1, v1, v4, vcc
	v_mul_lo_u32 v4, v2, v1
	v_add_u32_e32 v2, v4, v2
	v_cmp_ne_u32_e32 vcc, v3, v2
	s_and_saveexec_b64 s[4:5], vcc
	s_xor_b64 s[4:5], exec, s[4:5]
	s_cbranch_execz .LBB0_56
	s_waitcnt lgkmcnt(0)
	buffer_inv sc1
	v_mov_b32_e32 v0, 0x2000
	global_load_dword v0, v0, s[2:3] offset:1024 sc1
	s_add_u32 s10, s2, 0x2400
	s_addc_u32 s11, s3, 0
	s_waitcnt vmcnt(0)
	v_cmp_eq_u32_e32 vcc, v0, v1
	s_and_saveexec_b64 s[6:7], vcc
	s_cbranch_execz .LBB0_55
	s_mov_b32 s33, 1
	s_mov_b64 s[12:13], 0
	v_mov_b32_e32 v0, 0
	s_branch .LBB0_46

.LBB0_55:
	s_or_b64 exec, exec, s[6:7]
	s_waitcnt vmcnt(0)
	s_waitcnt vmcnt(0)
.LBB0_56:
	s_andn2_saveexec_b64 s[4:5], s[4:5]
	s_cbranch_execz .LBB0_76
	s_mov_b64 s[4:5], exec
	buffer_wbl2 sc1
	buffer_inv sc1
	s_waitcnt lgkmcnt(0)
	s_waitcnt vmcnt(0)
	v_mbcnt_lo_u32_b32 v1, s4, 0
	v_mbcnt_hi_u32_b32 v1, s5, v1
	v_cmp_eq_u32_e32 vcc, 0, v1
	s_and_saveexec_b64 s[6:7], vcc
	s_cbranch_execz .LBB0_59
	s_bcnt1_i32_b64 s4, s[4:5]
	v_mov_b32_e32 v2, 0x3000
	v_mov_b32_e32 v3, s4
	global_atomic_add v2, v2, v3, s[70:71] offset:1024 sc0

.LBB0_73:
	s_or_b64 exec, exec, s[4:5]
	s_mov_b64 s[4:5], exec
	v_mbcnt_lo_u32_b32 v0, s4, 0
	v_mbcnt_hi_u32_b32 v0, s5, v0
	v_cmp_eq_u32_e32 vcc, 0, v0
	s_waitcnt vmcnt(0)
	s_and_saveexec_b64 s[6:7], vcc
	s_cbranch_execz .LBB0_75
	s_bcnt1_i32_b64 s4, s[4:5]
	v_mov_b32_e32 v0, 0x2000
	v_mov_b32_e32 v1, s4
	global_atomic_add v0, v1, s[2:3] offset:1024

.LBB0_192:
	s_or_b64 exec, exec, s[10:11]
	v_cvt_f32_u32_e32 v4, v2
	s_waitcnt vmcnt(0)
	v_readfirstlane_b32 s4, v3
	v_sub_u32_e32 v3, 0, v2
	v_rcp_iflag_f32_e32 v4, v4
	v_add_u32_e32 v5, s4, v1
	v_mul_f32_e32 v4, 0x4f7ffffe, v4
	v_cvt_u32_f32_e32 v4, v4
	v_mul_lo_u32 v1, v3, v4
	v_mul_hi_u32 v1, v4, v1
	v_add_u32_e32 v1, v4, v1
	v_mul_hi_u32 v1, v5, v1
	v_mul_lo_u32 v3, v1, v2
	v_sub_u32_e32 v3, v5, v3
	v_add_u32_e32 v4, 1, v1
	v_cmp_ge_u32_e32 vcc, v3, v2
	s_nop 1
	v_cndmask_b32_e32 v1, v1, v4, vcc
	v_sub_u32_e32 v4, v3, v2
	v_cndmask_b32_e32 v3, v3, v4, vcc
	v_add_u32_e32 v4, 1, v1
	v_cmp_ge_u32_e32 vcc, v3, v2
	v_add_u32_e32 v3, 1, v5
	s_nop 0
	v_cndmask_b32_e32 v1, v1, v4, vcc
	v_mul_lo_u32 v4, v2, v1
	v_add_u32_e32 v2, v4, v2
	v_cmp_ne_u32_e32 vcc, v3, v2
	s_and_saveexec_b64 s[4:5], vcc
	s_xor_b64 s[4:5], exec, s[4:5]
	s_cbranch_execz .LBB0_206
	s_waitcnt lgkmcnt(0)
	buffer_inv sc1
	v_mov_b32_e32 v0, 0x2000
	global_load_dword v0, v0, s[2:3] offset:1024 sc1
	s_add_u32 s12, s2, 0x2400
	s_addc_u32 s13, s3, 0
	s_waitcnt vmcnt(0)
	v_cmp_eq_u32_e32 vcc, v0, v1
	s_and_saveexec_b64 s[10:11], vcc
	s_cbranch_execz .LBB0_205
	s_mov_b32 s26, 1
	s_mov_b64 s[14:15], 0
	v_mov_b32_e32 v0, 0
	s_branch .LBB0_196

.LBB0_205:
	s_or_b64 exec, exec, s[10:11]
	s_waitcnt vmcnt(0)
	s_waitcnt vmcnt(0)
.LBB0_206:
	s_andn2_saveexec_b64 s[4:5], s[4:5]
	s_cbranch_execz .LBB0_226
	s_mov_b64 s[4:5], exec
	buffer_wbl2 sc1
	buffer_inv sc1
	s_waitcnt lgkmcnt(0)
	s_waitcnt vmcnt(0)
	v_mbcnt_lo_u32_b32 v1, s4, 0
	v_mbcnt_hi_u32_b32 v1, s5, v1
	v_cmp_eq_u32_e32 vcc, 0, v1
	s_and_saveexec_b64 s[10:11], vcc
	s_cbranch_execz .LBB0_209
	s_bcnt1_i32_b64 s4, s[4:5]
	v_mov_b32_e32 v2, 0x3000
	v_mov_b32_e32 v3, s4
	global_atomic_add v2, v2, v3, s[70:71] offset:1024 sc0

.LBB0_223:
	s_or_b64 exec, exec, s[4:5]
	s_mov_b64 s[4:5], exec
	v_mbcnt_lo_u32_b32 v0, s4, 0
	v_mbcnt_hi_u32_b32 v0, s5, v0
	v_cmp_eq_u32_e32 vcc, 0, v0
	s_waitcnt vmcnt(0)
	s_and_saveexec_b64 s[10:11], vcc
	s_cbranch_execz .LBB0_225
	s_bcnt1_i32_b64 s4, s[4:5]
	v_mov_b32_e32 v0, 0x2000
	v_mov_b32_e32 v1, s4
	global_atomic_add v0, v1, s[2:3] offset:1024

.LBB0_287:
	s_or_b64 exec, exec, s[10:11]
	v_cvt_f32_u32_e32 v4, v2
	s_waitcnt vmcnt(0)
	v_readfirstlane_b32 s4, v3
	v_sub_u32_e32 v3, 0, v2
	v_rcp_iflag_f32_e32 v4, v4
	v_add_u32_e32 v5, s4, v1
	v_mul_f32_e32 v4, 0x4f7ffffe, v4
	v_cvt_u32_f32_e32 v4, v4
	v_mul_lo_u32 v1, v3, v4
	v_mul_hi_u32 v1, v4, v1
	v_add_u32_e32 v1, v4, v1
	v_mul_hi_u32 v1, v5, v1
	v_mul_lo_u32 v3, v1, v2
	v_sub_u32_e32 v3, v5, v3
	v_add_u32_e32 v4, 1, v1
	v_cmp_ge_u32_e32 vcc, v3, v2
	s_nop 1
	v_cndmask_b32_e32 v1, v1, v4, vcc
	v_sub_u32_e32 v4, v3, v2
	v_cndmask_b32_e32 v3, v3, v4, vcc
	v_add_u32_e32 v4, 1, v1
	v_cmp_ge_u32_e32 vcc, v3, v2
	v_add_u32_e32 v3, 1, v5
	s_nop 0
	v_cndmask_b32_e32 v1, v1, v4, vcc
	v_mul_lo_u32 v4, v2, v1
	v_add_u32_e32 v2, v4, v2
	v_cmp_ne_u32_e32 vcc, v3, v2
	s_and_saveexec_b64 s[4:5], vcc
	s_xor_b64 s[4:5], exec, s[4:5]
	s_cbranch_execz .LBB0_301
	s_waitcnt lgkmcnt(0)
	buffer_inv sc1
	v_mov_b32_e32 v0, 0x2000
	global_load_dword v0, v0, s[2:3] offset:1024 sc1
	s_add_u32 s12, s2, 0x2400
	s_addc_u32 s13, s3, 0
	s_waitcnt vmcnt(0)
	v_cmp_eq_u32_e32 vcc, v0, v1
	s_and_saveexec_b64 s[10:11], vcc
	s_cbranch_execz .LBB0_300
	s_mov_b32 s24, 1
	s_mov_b64 s[14:15], 0
	v_mov_b32_e32 v0, 0
	s_branch .LBB0_291

.LBB0_485:
	s_or_b64 exec, exec, s[8:9]
	v_cvt_f32_u32_e32 v4, v2
	s_waitcnt vmcnt(0)
	v_readfirstlane_b32 s4, v3
	v_sub_u32_e32 v3, 0, v2
	v_rcp_iflag_f32_e32 v4, v4
	v_add_u32_e32 v5, s4, v1
	v_mul_f32_e32 v4, 0x4f7ffffe, v4
	v_cvt_u32_f32_e32 v4, v4
	v_mul_lo_u32 v1, v3, v4
	v_mul_hi_u32 v1, v4, v1
	v_add_u32_e32 v1, v4, v1
	v_mul_hi_u32 v1, v5, v1
	v_mul_lo_u32 v3, v1, v2
	v_sub_u32_e32 v3, v5, v3
	v_add_u32_e32 v4, 1, v1
	v_cmp_ge_u32_e32 vcc, v3, v2
	s_nop 1
	v_cndmask_b32_e32 v1, v1, v4, vcc
	v_sub_u32_e32 v4, v3, v2
	v_cndmask_b32_e32 v3, v3, v4, vcc
	v_add_u32_e32 v4, 1, v1
	v_cmp_ge_u32_e32 vcc, v3, v2
	v_add_u32_e32 v3, 1, v5
	s_nop 0
	v_cndmask_b32_e32 v1, v1, v4, vcc
	v_mul_lo_u32 v4, v2, v1
	v_add_u32_e32 v2, v4, v2
	v_cmp_ne_u32_e32 vcc, v3, v2
	s_and_saveexec_b64 s[4:5], vcc
	s_xor_b64 s[4:5], exec, s[4:5]
	s_cbranch_execz .LBB0_499
	s_waitcnt lgkmcnt(0)
	buffer_inv sc1
	v_mov_b32_e32 v0, 0x2000
	global_load_dword v0, v0, s[2:3] offset:1024 sc1
	s_add_u32 s10, s2, 0x2400
	s_addc_u32 s11, s3, 0
	s_waitcnt vmcnt(0)
	v_cmp_eq_u32_e32 vcc, v0, v1
	s_and_saveexec_b64 s[8:9], vcc
	s_cbranch_execz .LBB0_498
	s_mov_b32 s22, 1
	s_mov_b64 s[12:13], 0
	v_mov_b32_e32 v0, 0
	s_branch .LBB0_489

.LBB0_498:
	s_or_b64 exec, exec, s[8:9]
	s_waitcnt vmcnt(0)
	s_waitcnt vmcnt(0)
.LBB0_499:
	s_andn2_saveexec_b64 s[4:5], s[4:5]
	s_cbranch_execz .LBB0_519
	s_mov_b64 s[4:5], exec
	buffer_wbl2 sc1
	buffer_inv sc1
	s_waitcnt lgkmcnt(0)
	s_waitcnt vmcnt(0)
	v_mbcnt_lo_u32_b32 v1, s4, 0
	v_mbcnt_hi_u32_b32 v1, s5, v1
	v_cmp_eq_u32_e32 vcc, 0, v1
	s_and_saveexec_b64 s[8:9], vcc
	s_cbranch_execz .LBB0_502
	s_bcnt1_i32_b64 s4, s[4:5]
	v_mov_b32_e32 v2, 0x3000
	v_mov_b32_e32 v3, s4
	global_atomic_add v2, v2, v3, s[70:71] offset:1024 sc0

.LBB0_516:
	s_or_b64 exec, exec, s[4:5]
	s_mov_b64 s[4:5], exec
	v_mbcnt_lo_u32_b32 v0, s4, 0
	v_mbcnt_hi_u32_b32 v0, s5, v0
	v_cmp_eq_u32_e32 vcc, 0, v0
	s_waitcnt vmcnt(0)
	s_and_saveexec_b64 s[8:9], vcc
	s_cbranch_execz .LBB0_518
	s_bcnt1_i32_b64 s4, s[4:5]
	v_mov_b32_e32 v0, 0x2000
	v_mov_b32_e32 v1, s4
	global_atomic_add v0, v1, s[2:3] offset:1024

.LBB0_544:
	s_or_b64 exec, exec, s[6:7]
	v_cvt_f32_u32_e32 v4, v2
	s_waitcnt vmcnt(0)
	v_readfirstlane_b32 s4, v3
	v_sub_u32_e32 v3, 0, v2
	v_rcp_iflag_f32_e32 v4, v4
	v_add_u32_e32 v5, s4, v1
	v_mul_f32_e32 v4, 0x4f7ffffe, v4
	v_cvt_u32_f32_e32 v4, v4
	v_mul_lo_u32 v1, v3, v4
	v_mul_hi_u32 v1, v4, v1
	v_add_u32_e32 v1, v4, v1
	v_mul_hi_u32 v1, v5, v1
	v_mul_lo_u32 v3, v1, v2
	v_sub_u32_e32 v3, v5, v3
	v_add_u32_e32 v4, 1, v1
	v_cmp_ge_u32_e32 vcc, v3, v2
	s_nop 1
	v_cndmask_b32_e32 v1, v1, v4, vcc
	v_sub_u32_e32 v4, v3, v2
	v_cndmask_b32_e32 v3, v3, v4, vcc
	v_add_u32_e32 v4, 1, v1
	v_cmp_ge_u32_e32 vcc, v3, v2
	v_add_u32_e32 v3, 1, v5
	s_nop 0
	v_cndmask_b32_e32 v1, v1, v4, vcc
	v_mul_lo_u32 v4, v2, v1
	v_add_u32_e32 v2, v4, v2
	v_cmp_ne_u32_e32 vcc, v3, v2
	s_and_saveexec_b64 s[4:5], vcc
	s_xor_b64 s[4:5], exec, s[4:5]
	s_cbranch_execz .LBB0_558
	s_waitcnt lgkmcnt(0)
	buffer_inv sc1
	v_mov_b32_e32 v0, 0x2000
	global_load_dword v0, v0, s[2:3] offset:1024 sc1
	s_add_u32 s8, s2, 0x2400
	s_addc_u32 s9, s3, 0
	s_waitcnt vmcnt(0)
	v_cmp_eq_u32_e32 vcc, v0, v1
	s_and_saveexec_b64 s[6:7], vcc
	s_cbranch_execz .LBB0_557
	s_mov_b32 s20, 1
	s_mov_b64 s[10:11], 0
	v_mov_b32_e32 v0, 0
	s_branch .LBB0_548
